# hyena units (context + latent pair): loads into an unused register touch the next stages' filter rows and gate-stream blocks ahead of each long compute loop so later stage loads hit in cache
# baseline (speedup 1.0000x reference)
.LBB0_646:
	v_mov_b32_e32 v2, v0
	s_load_dwordx4 s[4:7], s[66:67], 0x58
	v_readlane_b32 s1, v254, 46
	s_add_i32 s10, s1, s57
	v_readlane_b32 s1, v254, 10
	s_mov_b32 s11, s23
	s_waitcnt lgkmcnt(0)
	s_add_u32 s1, s4, s1
	v_readlane_b32 s4, v254, 12
	s_addc_u32 s18, s5, s4
	v_readlane_b32 s4, v254, 5
	s_add_u32 s19, s6, s4
	v_readlane_b32 s4, v254, 14
	s_addc_u32 s33, s7, s4
	s_movk_i32 s4, 0x200
	v_cmp_gt_i32_e32 vcc, s4, v2
	v_ashrrev_i32_e32 v6, 1, v2
	v_lshlrev_b32_e32 v7, 4, v2
	s_waitcnt vmcnt(0)
	s_barrier
	v_readlane_b32 s42, v254, 42
	v_readlane_b32 s43, v254, 43
	s_lshl_b64 s[60:61], s[10:11], 10
	s_add_u32 s42, s42, s60
	s_addc_u32 s43, s43, s61
	v_lshlrev_b32_e32 v40, 2, v0
	s_add_i32 s60, s10, 0x100
	s_mov_b32 s61, 0
	s_lshl_b64 s[60:61], s[60:61], 13
	s_add_u32 s60, s50, s60
	s_addc_u32 s61, s51, s61
	v_lshlrev_b32_e32 v41, 4, v0
	global_load_dword v255, v40, s[42:43]
	global_load_dword v255, v41, s[60:61]
	s_add_u32 s42, s42, 0x40000
	s_addc_u32 s43, s43, 0
	s_add_u32 s60, s60, 0x200000
	s_addc_u32 s61, s61, 0
	global_load_dword v255, v40, s[42:43]
	global_load_dword v255, v41, s[60:61]
	s_and_saveexec_b64 s[4:5], vcc
	s_cbranch_execz .LBB0_648
	v_lshlrev_b32_e32 v4, 8, v2
	s_lshl_b64 s[6:7], s[10:11], 13
	v_and_b32_e32 v4, 0xf00, v4
	v_and_b32_e32 v5, -8, v6
	s_add_u32 s6, s50, s6
	v_add_u32_e32 v4, v4, v5
	s_addc_u32 s7, s51, s7
	v_ashrrev_i32_e32 v5, 31, v4
	v_lshl_add_u64 v[12:13], v[4:5], 1, s[6:7]
	global_load_dwordx4 v[8:11], v[12:13], off
	global_load_ushort v5, v[12:13], off offset:16
	s_movk_i32 s6, 0x1ef
	global_load_ushort v12, v[12:13], off offset:-2
	v_cmp_lt_i32_e32 vcc, s6, v2
	s_lshl_b64 s[6:7], s[10:11], 2
	s_add_u32 s12, s19, s6
	s_addc_u32 s13, s33, s7
	v_cndmask_b32_e64 v4, 1.0, 0, vcc
	v_cmp_lt_i32_e32 vcc, 15, v2
	s_add_u32 s6, s1, s6
	s_addc_u32 s7, s18, s7
	v_add_u32_e32 v3, 0, v7
	s_waitcnt vmcnt(2)
	v_lshlrev_b32_e32 v17, 16, v8
	s_waitcnt vmcnt(1)
	v_lshlrev_b32_e32 v5, 16, v5
	v_mul_f32_e32 v5, v4, v5
	v_cndmask_b32_e64 v4, 0, 1.0, vcc
	s_waitcnt vmcnt(0)
	v_lshlrev_b32_e32 v12, 16, v12
	v_mul_f32_e32 v16, v4, v12
	global_load_dword v4, v131, s[12:13]
	global_load_dword v12, v1, s[6:7] offset:2048
	global_load_dword v18, v131, s[6:7] offset:3072
	global_load_dword v20, v131, s[6:7]
	v_and_b32_e32 v8, 0xffff0000, v8
	v_and_b32_e32 v25, 16, v10
	v_and_b32_e32 v24, 0xffff0000, v9
	v_lshlrev_b32_e32 v9, 16, v9
	v_lshlrev_b32_e32 v22, 16, v11
	v_and_b32_e32 v14, 0xffff0000, v10
	v_and_b32_e32 v23, 0xffff0000, v11
	v_mov_b32_e32 v15, v22
	v_lshlrev_b32_e32 v11, 16, v10
	v_mov_b32_e32 v10, v24
	s_waitcnt vmcnt(0)
	v_pk_fma_f32 v[26:27], v[20:21], v[16:17], v[4:5] op_sel_hi:[0,1,0]
	v_mov_b32_e32 v16, v17
	v_mov_b32_e32 v17, v8
	v_pk_fma_f32 v[16:17], v[18:19], v[16:17], v[26:27] op_sel_hi:[0,1,1]
	v_pk_fma_f32 v[16:17], v[12:13], v[8:9], v[16:17] op_sel_hi:[0,1,1]
	v_pk_fma_f32 v[26:27], v[20:21], v[8:9], v[4:5] op_sel_hi:[0,1,0]
	v_pk_mov_b32 v[8:9], v[8:9], v[24:25] op_sel:[1,0]
	s_nop 0
	v_pk_fma_f32 v[8:9], v[18:19], v[8:9], v[26:27] op_sel_hi:[0,1,1]
	v_pk_fma_f32 v[24:25], v[12:13], v[10:11], v[8:9] op_sel_hi:[0,1,1]
	v_pk_fma_f32 v[8:9], v[20:21], v[10:11], v[4:5] op_sel_hi:[0,1,0]
	v_pk_mov_b32 v[10:11], v[10:11], v[14:15] op_sel:[1,0]
	s_nop 0
	v_pk_fma_f32 v[8:9], v[18:19], v[10:11], v[8:9] op_sel_hi:[0,1,1]
	v_pk_fma_f32 v[10:11], v[12:13], v[14:15], v[8:9] op_sel_hi:[0,1,1]
	v_pk_fma_f32 v[8:9], v[20:21], v[14:15], v[4:5] op_sel_hi:[0,1,0]
	v_pk_fma_f32 v[8:9], v[18:19], v[22:23], v[8:9] op_sel_hi:[0,1,1]
	v_mov_b32_e32 v4, v23
	v_pk_fma_f32 v[4:5], v[12:13], v[4:5], v[8:9] op_sel_hi:[0,1,1]
	v_cvt_pk_bf16_f32 v8, v16, v17
	v_cvt_pk_bf16_f32 v9, v24, v25
	v_cvt_pk_bf16_f32 v10, v10, v11
	v_cvt_pk_bf16_f32 v11, v4, v5
	ds_write_b128 v3, v[8:11] offset:20480

.LBB0_698:
	s_andn2_b64 vcc, exec, s[4:5]
	s_cbranch_vccnz .LBB0_789
	v_mov_b32_e32 v136, v0
	s_load_dwordx4 s[4:7], s[66:67], 0x58
	s_lshl_b32 s1, s57, 1
	s_add_i32 s84, s44, s1
	v_readlane_b32 s1, v254, 10
	s_mov_b32 s85, s23
	s_waitcnt lgkmcnt(0)
	s_add_u32 s1, s4, s1
	v_readlane_b32 s4, v254, 12
	s_addc_u32 s4, s5, s4
	v_readlane_b32 s5, v254, 5
	s_add_u32 s5, s6, s5
	v_readlane_b32 s6, v254, 14
	s_addc_u32 s6, s7, s6
	s_lshl_b64 s[90:91], s[84:85], 2
	s_add_u32 s86, s1, s90
	v_lshlrev_b32_e32 v2, 11, v136
	v_add_u32_e32 v31, 0x200, v136
	s_addc_u32 s87, s4, s91
	v_and_b32_e32 v53, 0x7800, v2
	v_ashrrev_i32_e32 v2, 1, v31
	v_add_u32_e32 v138, 0x400, v136
	s_add_u32 s88, s5, s90
	v_and_b32_e32 v2, -8, v2
	s_movk_i32 s1, 0xe00
	v_ashrrev_i32_e32 v4, 1, v138
	s_addc_u32 s89, s6, s91
	s_lshl_b64 s[4:5], s[84:85], 16
	v_add_u32_e32 v2, v2, v53
	v_cmp_gt_i32_e64 s[14:15], s1, v136
	v_and_b32_e32 v4, -8, v4
	s_movk_i32 s1, 0xc00
	s_add_u32 s92, s58, s4
	v_cndmask_b32_e64 v2, 8, v2, s[14:15]
	v_add_u32_e32 v4, v4, v53
	v_cmp_gt_i32_e64 s[12:13], s1, v136
	s_addc_u32 s93, s59, s5
	v_ashrrev_i32_e32 v3, 31, v2
	v_cndmask_b32_e64 v4, 8, v4, s[12:13]
	v_lshl_add_u64 v[2:3], v[2:3], 1, s[92:93]
	v_ashrrev_i32_e32 v5, 31, v4
	v_add_u32_e32 v140, 0x600, v136
	s_waitcnt vmcnt(0)
	s_barrier
	s_lshl_b64 s[60:61], s[84:85], 13
	s_add_u32 s60, s34, s60
	s_addc_u32 s61, s35, s61
	v_lshlrev_b32_e32 v245, 4, v0
	global_load_dword v255, v245, s[60:61]
	global_load_dword v30, v1, s[86:87] offset:2048
	global_load_dword v34, v131, s[86:87]
	global_load_dword v32, v131, s[86:87] offset:3072
	global_load_dword v36, v131, s[88:89]
	v_lshl_add_u64 v[4:5], v[4:5], 1, s[92:93]
	global_load_dwordx4 v[26:29], v[2:3], off
	global_load_ushort v51, v[2:3], off offset:16
	global_load_ushort v49, v[4:5], off offset:-2
	global_load_ushort v52, v[2:3], off offset:-2
	v_ashrrev_i32_e32 v2, 1, v140
	v_and_b32_e32 v2, -8, v2
	s_movk_i32 s1, 0xa00
	v_add_u32_e32 v2, v2, v53
	v_cmp_gt_i32_e32 vcc, s1, v136
	v_add_u32_e32 v42, 0x800, v136
	s_movk_i32 s1, 0x800
	v_cndmask_b32_e32 v2, 8, v2, vcc
	v_ashrrev_i32_e32 v3, 31, v2
	v_lshl_add_u64 v[2:3], v[2:3], 1, s[92:93]
	global_load_dwordx4 v[22:25], v[4:5], off
	global_load_ushort v50, v[4:5], off offset:16
	global_load_ushort v47, v[2:3], off offset:-2
	v_ashrrev_i32_e32 v4, 1, v42
	v_and_b32_e32 v4, -8, v4
	v_add_u32_e32 v4, v4, v53
	v_cmp_gt_i32_e64 s[4:5], s1, v136
	v_add_u32_e32 v39, 0xa00, v136
	s_movk_i32 s1, 0x600
	v_cndmask_b32_e64 v4, 8, v4, s[4:5]
	v_ashrrev_i32_e32 v5, 31, v4
	v_lshl_add_u64 v[4:5], v[4:5], 1, s[92:93]
	global_load_dwordx4 v[18:21], v[2:3], off
	global_load_ushort v48, v[2:3], off offset:16
	global_load_ushort v45, v[4:5], off offset:-2
	v_ashrrev_i32_e32 v2, 1, v39
	v_and_b32_e32 v2, -8, v2
	v_add_u32_e32 v2, v2, v53
	v_cmp_gt_i32_e64 s[6:7], s1, v136
	v_add_u32_e32 v35, 0xc00, v136
	s_movk_i32 s1, 0x400
	v_cndmask_b32_e64 v2, 8, v2, s[6:7]
	v_ashrrev_i32_e32 v3, 31, v2
	v_lshl_add_u64 v[2:3], v[2:3], 1, s[92:93]
	global_load_dwordx4 v[14:17], v[4:5], off
	global_load_ushort v46, v[4:5], off offset:16
	global_load_ushort v43, v[2:3], off offset:-2
	v_ashrrev_i32_e32 v4, 1, v35
	v_and_b32_e32 v4, -8, v4
	v_add_u32_e32 v4, v4, v53
	v_cmp_gt_i32_e64 s[8:9], s1, v136
	v_add_u32_e32 v33, 0xe00, v136
	s_movk_i32 s1, 0x200
	v_cndmask_b32_e64 v4, 8, v4, s[8:9]
	v_ashrrev_i32_e32 v5, 31, v4
	v_lshl_add_u64 v[4:5], v[4:5], 1, s[92:93]
	global_load_dwordx4 v[10:13], v[2:3], off
	global_load_ushort v44, v[2:3], off offset:16
	global_load_ushort v40, v[4:5], off offset:-2
	v_ashrrev_i32_e32 v2, 1, v33
	v_and_b32_e32 v2, -8, v2
	v_add_u32_e32 v2, v2, v53
	v_cmp_gt_i32_e64 s[10:11], s1, v136
	v_cmp_gt_i32_e64 s[16:17], s28, v136
	s_nop 0
	v_cndmask_b32_e64 v2, 8, v2, s[10:11]
	v_ashrrev_i32_e32 v3, 31, v2
	v_lshl_add_u64 v[54:55], v[2:3], 1, s[92:93]
	global_load_dwordx4 v[6:9], v[4:5], off
	global_load_ushort v41, v[4:5], off offset:16
	global_load_ushort v38, v[54:55], off offset:-2
	s_nop 0
	global_load_dwordx4 v[2:5], v[54:55], off
	global_load_ushort v37, v[54:55], off offset:16
	s_and_saveexec_b64 s[18:19], s[16:17]
	s_cbranch_execz .LBB0_707
	v_ashrrev_i32_e32 v54, 1, v136
	v_and_b32_e32 v54, -8, v54
	v_add_u32_e32 v54, v54, v53
	v_ashrrev_i32_e32 v55, 31, v54
	v_lshl_add_u64 v[58:59], v[54:55], 1, s[92:93]
	global_load_dwordx4 v[54:57], v[58:59], off
	global_load_ushort v53, v[58:59], off offset:-2
	v_cmp_lt_i32_e64 s[16:17], 15, v136
	s_movk_i32 s1, 0xfef
	s_waitcnt vmcnt(1)
	v_lshlrev_b32_e32 v61, 16, v54
	s_waitcnt vmcnt(0)
	v_lshlrev_b32_e32 v53, 16, v53
	v_cndmask_b32_e64 v60, 0, 1.0, s[16:17]
	v_mul_f32_e32 v60, v60, v53
	global_load_ushort v53, v[58:59], off offset:16
	v_and_b32_e32 v54, 0xffff0000, v54
	v_pk_fma_f32 v[68:69], v[34:35], v[60:61], v[36:37] op_sel_hi:[0,1,0]
	v_mov_b32_e32 v60, v61
	v_mov_b32_e32 v61, v54
	v_and_b32_e32 v67, 16, v56
	v_and_b32_e32 v66, 0xffff0000, v55
	v_lshlrev_b32_e32 v55, 16, v55
	v_pk_fma_f32 v[60:61], v[32:33], v[60:61], v[68:69] op_sel_hi:[0,1,1]
	v_lshlrev_b32_e32 v64, 16, v57
	v_pk_fma_f32 v[60:61], v[30:31], v[54:55], v[60:61] op_sel_hi:[0,1,1]
	v_pk_fma_f32 v[68:69], v[34:35], v[54:55], v[36:37] op_sel_hi:[0,1,0]
	v_pk_mov_b32 v[54:55], v[54:55], v[66:67] op_sel:[1,0]
	v_and_b32_e32 v62, 0xffff0000, v56
	v_and_b32_e32 v65, 0xffff0000, v57
	v_mov_b32_e32 v63, v64
	v_lshlrev_b32_e32 v57, 16, v56
	v_mov_b32_e32 v56, v66
	v_pk_fma_f32 v[54:55], v[32:33], v[54:55], v[68:69] op_sel_hi:[0,1,1]
	v_pk_fma_f32 v[66:67], v[30:31], v[56:57], v[54:55] op_sel_hi:[0,1,1]
	v_pk_fma_f32 v[54:55], v[34:35], v[56:57], v[36:37] op_sel_hi:[0,1,0]
	v_pk_mov_b32 v[56:57], v[56:57], v[62:63] op_sel:[1,0]
	v_cmp_lt_i32_e64 s[16:17], s1, v136
	v_pk_fma_f32 v[54:55], v[32:33], v[56:57], v[54:55] op_sel_hi:[0,1,1]
	v_pk_fma_f32 v[56:57], v[30:31], v[62:63], v[54:55] op_sel_hi:[0,1,1]
	v_cndmask_b32_e64 v58, 1.0, 0, s[16:17]
	v_pk_fma_f32 v[54:55], v[34:35], v[62:63], v[36:37] op_sel_hi:[0,1,0]
	v_pk_fma_f32 v[54:55], v[32:33], v[64:65], v[54:55] op_sel_hi:[0,1,1]
	v_cvt_pk_bf16_f32 v56, v56, v57
	s_waitcnt vmcnt(0)
	v_lshlrev_b32_e32 v53, 16, v53
	v_mul_f32_e32 v59, v58, v53
	v_mov_b32_e32 v58, v65
	v_pk_fma_f32 v[58:59], v[30:31], v[58:59], v[54:55] op_sel_hi:[0,1,1]
	v_cvt_pk_bf16_f32 v54, v60, v61
	v_cvt_pk_bf16_f32 v55, v66, v67
	v_cvt_pk_bf16_f32 v57, v58, v59
	v_lshl_add_u32 v53, v136, 4, 0
	ds_write_b128 v53, v[54:57] offset:20480
	s_or_b64 exec, exec, s[18:19]
	s_and_saveexec_b64 s[16:17], s[14:15]
	s_cbranch_execnz .LBB0_708

.LBB0_740:
	s_or_b64 exec, exec, s[38:39]
	s_waitcnt lgkmcnt(0)
	s_barrier
	ds_read2_b32 v[66:67], v152 offset1:1
	ds_read2_b32 v[68:69], v153 offset1:1
	ds_read2_b32 v[70:71], v154 offset1:1
	ds_read2_b32 v[72:73], v155 offset1:1
	ds_read2_b32 v[74:75], v156 offset1:1
	ds_read2_b32 v[76:77], v157 offset1:1
	ds_read2_b32 v[78:79], v158 offset1:1
	ds_read2_b32 v[80:81], v159 offset1:1
	ds_read2_b32 v[82:83], v160 offset1:1
	ds_read2_b32 v[84:85], v161 offset1:1
	ds_read2_b32 v[86:87], v162 offset1:1
	ds_read2_b32 v[88:89], v163 offset1:1
	ds_read2_b32 v[94:95], v164 offset1:1
	ds_read2_b32 v[96:97], v165 offset1:1
	ds_read2_b32 v[98:99], v166 offset1:1
	ds_read2_b32 v[100:101], v167 offset1:1
	ds_read2_b32 v[106:107], v168 offset1:1
	ds_read2_b32 v[108:109], v169 offset1:1
	ds_read2_b32 v[110:111], v170 offset1:1
	ds_read2_b32 v[112:113], v171 offset1:1
	ds_read2_b32 v[114:115], v172 offset1:1
	ds_read2_b32 v[116:117], v173 offset1:1
	ds_read2_b32 v[118:119], v174 offset1:1
	ds_read2_b32 v[120:121], v175 offset1:1
	ds_read2_b32 v[122:123], v178 offset1:1
	ds_read2_b32 v[124:125], v179 offset1:1
	ds_read2_b32 v[90:91], v180 offset1:1
	ds_read2_b32 v[92:93], v181 offset1:1
	ds_read2_b32 v[126:127], v150 offset1:1
	ds_read2_b32 v[128:129], v151 offset1:1
	ds_read2_b32 v[102:103], v146 offset1:1
	ds_read2_b32 v[104:105], v146 offset0:2 offset1:3
	ds_read_b128 v[132:135], v221 offset:20480
	v_mov_b32_e32 v62, 0
	s_xor_b64 s[90:91], s[90:91], -1
	s_mov_b32 s38, -8
	s_mov_b32 s39, 32
	v_mov_b32_e32 v130, v217
	v_mov_b32_e32 v142, v201
	v_mov_b32_e32 v63, v62
	v_mov_b32_e32 v64, v62
	v_mov_b32_e32 v65, v62
	v_mov_b32_e32 v58, v62
	v_mov_b32_e32 v59, v62
	v_mov_b32_e32 v60, v62
	v_mov_b32_e32 v61, v62
	v_mov_b32_e32 v54, v62
	v_mov_b32_e32 v55, v62
	v_mov_b32_e32 v56, v62
	v_mov_b32_e32 v57, v62
	v_mov_b32_e32 v50, v62
	v_mov_b32_e32 v51, v62
	v_mov_b32_e32 v52, v62
	v_mov_b32_e32 v53, v62
	v_mov_b32_e32 v46, v62
	v_mov_b32_e32 v47, v62
	v_mov_b32_e32 v48, v62
	v_mov_b32_e32 v49, v62
	v_mov_b32_e32 v42, v62
	v_mov_b32_e32 v43, v62
	v_mov_b32_e32 v44, v62
	v_mov_b32_e32 v45, v62
	v_mov_b32_e32 v38, v62
	v_mov_b32_e32 v39, v62
	v_mov_b32_e32 v40, v62
	v_mov_b32_e32 v41, v62
	v_mov_b32_e32 v34, v62
	v_mov_b32_e32 v35, v62
	v_mov_b32_e32 v36, v62
	s_waitcnt vmcnt(0)
	v_mov_b32_e32 v37, v62
	v_mov_b32_e32 v30, v62
	v_mov_b32_e32 v31, v62
	v_mov_b32_e32 v32, v62
	v_mov_b32_e32 v33, v62
	v_mov_b32_e32 v26, v62
	v_mov_b32_e32 v27, v62
	v_mov_b32_e32 v28, v62
	v_mov_b32_e32 v29, v62
	v_mov_b32_e32 v22, v62
	v_mov_b32_e32 v23, v62
	v_mov_b32_e32 v24, v62
	v_mov_b32_e32 v25, v62
	v_mov_b32_e32 v18, v62
	v_mov_b32_e32 v19, v62
	v_mov_b32_e32 v20, v62
	v_mov_b32_e32 v21, v62
	v_mov_b32_e32 v14, v62
	v_mov_b32_e32 v15, v62
	v_mov_b32_e32 v16, v62
	v_mov_b32_e32 v17, v62
	v_mov_b32_e32 v10, v62
	v_mov_b32_e32 v11, v62
	v_mov_b32_e32 v12, v62
	v_mov_b32_e32 v13, v62
	v_mov_b32_e32 v6, v62
	v_mov_b32_e32 v7, v62
	v_mov_b32_e32 v8, v62
	v_mov_b32_e32 v9, v62
	v_mov_b32_e32 v2, v62
	v_mov_b32_e32 v3, v62
	v_mov_b32_e32 v4, v62
	v_mov_b32_e32 v5, v62
	s_lshl_b32 s92, s22, 8
	s_add_i32 s92, s42, s92
	s_mov_b32 s93, 0
	s_lshl_b64 s[92:93], s[92:93], 16
	s_add_u32 s92, s58, s92
	s_addc_u32 s93, s59, s93
	v_lshlrev_b32_e32 v244, 6, v0
	v_lshlrev_b32_e32 v245, 4, v0
	global_load_dword v255, v244, s[92:93]
	s_add_u32 s60, s92, 0x8000
	s_addc_u32 s61, s93, 0
	global_load_dword v255, v244, s[60:61]
	s_add_i32 s60, s22, 1
	s_mov_b32 s61, 0
	s_lshl_b64 s[60:61], s[60:61], 21
	s_add_u32 s60, s64, s60
	s_addc_u32 s61, s94, s61
	global_load_dword v255, v245, s[60:61]
	s_add_i32 s92, s42, 0xffffff01
	s_mov_b32 s93, 0
	s_lshl_b64 s[92:93], s[92:93], 16
	s_add_u32 s92, s58, s92
	s_addc_u32 s93, s59, s93
	global_load_dword v255, v244, s[92:93]
	s_add_u32 s92, s92, 0x8000
	s_addc_u32 s93, s93, 0
	global_load_dword v255, v244, s[92:93]
	s_add_u32 s60, s64, 0x2000
	s_addc_u32 s61, s94, 0
	global_load_dword v255, v245, s[60:61]

.LBB0_784:
	s_or_b64 exec, exec, s[38:39]
	s_waitcnt lgkmcnt(0)
	s_barrier
	ds_read2_b32 v[70:71], v152 offset1:1
	ds_read2_b32 v[72:73], v153 offset1:1
	ds_read2_b32 v[66:67], v154 offset1:1
	ds_read2_b32 v[68:69], v155 offset1:1
	ds_read2_b32 v[74:75], v156 offset1:1
	ds_read2_b32 v[76:77], v157 offset1:1
	ds_read2_b32 v[78:79], v158 offset1:1
	ds_read2_b32 v[80:81], v159 offset1:1
	ds_read2_b32 v[82:83], v160 offset1:1
	ds_read2_b32 v[84:85], v161 offset1:1
	ds_read2_b32 v[86:87], v162 offset1:1
	ds_read2_b32 v[88:89], v163 offset1:1
	ds_read2_b32 v[94:95], v164 offset1:1
	ds_read2_b32 v[96:97], v165 offset1:1
	ds_read2_b32 v[98:99], v166 offset1:1
	ds_read2_b32 v[100:101], v167 offset1:1
	ds_read2_b32 v[106:107], v168 offset1:1
	ds_read2_b32 v[108:109], v169 offset1:1
	ds_read2_b32 v[110:111], v170 offset1:1
	ds_read2_b32 v[112:113], v171 offset1:1
	ds_read2_b32 v[114:115], v172 offset1:1
	ds_read2_b32 v[116:117], v173 offset1:1
	ds_read2_b32 v[118:119], v174 offset1:1
	ds_read2_b32 v[120:121], v175 offset1:1
	ds_read2_b32 v[122:123], v178 offset1:1
	ds_read2_b32 v[124:125], v179 offset1:1
	ds_read2_b32 v[90:91], v180 offset1:1
	ds_read2_b32 v[92:93], v181 offset1:1
	ds_read2_b32 v[126:127], v150 offset1:1
	ds_read2_b32 v[128:129], v151 offset1:1
	ds_read2_b32 v[102:103], v146 offset1:1
	ds_read2_b32 v[104:105], v146 offset0:2 offset1:3
	ds_read_b128 v[132:135], v221
	v_mov_b32_e32 v62, 0
	s_xor_b64 s[90:91], s[90:91], -1
	s_mov_b32 s38, -8
	s_mov_b32 s39, 32
	v_mov_b32_e32 v130, v217
	v_mov_b32_e32 v142, v201
	v_mov_b32_e32 v63, v62
	v_mov_b32_e32 v64, v62
	v_mov_b32_e32 v65, v62
	v_mov_b32_e32 v58, v62
	v_mov_b32_e32 v59, v62
	v_mov_b32_e32 v60, v62
	v_mov_b32_e32 v61, v62
	v_mov_b32_e32 v54, v62
	v_mov_b32_e32 v55, v62
	v_mov_b32_e32 v56, v62
	v_mov_b32_e32 v57, v62
	v_mov_b32_e32 v50, v62
	v_mov_b32_e32 v51, v62
	v_mov_b32_e32 v52, v62
	v_mov_b32_e32 v53, v62
	v_mov_b32_e32 v46, v62
	v_mov_b32_e32 v47, v62
	v_mov_b32_e32 v48, v62
	v_mov_b32_e32 v49, v62
	v_mov_b32_e32 v42, v62
	v_mov_b32_e32 v43, v62
	v_mov_b32_e32 v44, v62
	v_mov_b32_e32 v45, v62
	v_mov_b32_e32 v38, v62
	v_mov_b32_e32 v39, v62
	v_mov_b32_e32 v40, v62
	s_waitcnt vmcnt(0)
	v_mov_b32_e32 v41, v62
	v_mov_b32_e32 v34, v62
	v_mov_b32_e32 v35, v62
	v_mov_b32_e32 v36, v62
	v_mov_b32_e32 v37, v62
	v_mov_b32_e32 v30, v62
	v_mov_b32_e32 v31, v62
	v_mov_b32_e32 v32, v62
	v_mov_b32_e32 v33, v62
	v_mov_b32_e32 v26, v62
	v_mov_b32_e32 v27, v62
	v_mov_b32_e32 v28, v62
	v_mov_b32_e32 v29, v62
	v_mov_b32_e32 v22, v62
	v_mov_b32_e32 v23, v62
	v_mov_b32_e32 v24, v62
	v_mov_b32_e32 v25, v62
	v_mov_b32_e32 v18, v62
	v_mov_b32_e32 v19, v62
	v_mov_b32_e32 v20, v62
	v_mov_b32_e32 v21, v62
	v_mov_b32_e32 v14, v62
	v_mov_b32_e32 v15, v62
	v_mov_b32_e32 v16, v62
	v_mov_b32_e32 v17, v62
	v_mov_b32_e32 v10, v62
	v_mov_b32_e32 v11, v62
	v_mov_b32_e32 v12, v62
	v_mov_b32_e32 v13, v62
	v_mov_b32_e32 v6, v62
	v_mov_b32_e32 v7, v62
	v_mov_b32_e32 v8, v62
	v_mov_b32_e32 v9, v62
	v_mov_b32_e32 v2, v62
	v_mov_b32_e32 v3, v62
	v_mov_b32_e32 v4, v62
	v_mov_b32_e32 v5, v62
	s_lshl_b32 s92, s22, 8
	s_add_i32 s92, s42, s92
	s_mov_b32 s93, 0
	s_lshl_b64 s[92:93], s[92:93], 16
	s_add_u32 s92, s58, s92
	s_addc_u32 s93, s59, s93
	v_lshlrev_b32_e32 v244, 6, v0
	v_lshlrev_b32_e32 v245, 4, v0
	global_load_dword v255, v244, s[92:93]
	s_add_u32 s60, s92, 0x8000
	s_addc_u32 s61, s93, 0
	global_load_dword v255, v244, s[60:61]
	s_add_i32 s60, s22, 1
	s_mov_b32 s61, 0
	s_lshl_b64 s[60:61], s[60:61], 21
	s_add_u32 s60, s94, s60
	s_addc_u32 s61, s64, s61
	global_load_dword v255, v245, s[60:61]
